# baseline (speedup 1.0000x reference)
.LBB2_20:
	s_mov_b64 exec, -1
	s_waitcnt lgkmcnt(0)
	s_barrier
	ds_read_b128 v[50:53], v111
	ds_read_b128 v[54:57], v111 offset:4096
	ds_read_b128 v[58:61], v111 offset:8192
	ds_read_b128 v[70:73], v111 offset:12288
	ds_read_b128 v[78:81], v124
	ds_read_b128 v[82:85], v124 offset:4096
	ds_read_b128 v[86:89], v124 offset:8192
	ds_read_b128 v[90:93], v124 offset:12288
	ds_read_b128 v[94:97], v125
	ds_read_b128 v[98:101], v125 offset:4096
	ds_read_b128 v[102:105], v125 offset:8192
	ds_read_b128 v[106:109], v125 offset:12288
	v_smfmac_f32_16x16x64_f16 v[62:65], v[0:3], a[0:7], v28
	v_smfmac_f32_16x16x64_f16 v[66:69], v[0:3], a[128:135], v28
	v_mov_b32_e32 v29, v128
	v_mov_b32_e32 v30, v129
	v_mov_b32_e32 v31, v130
	v_mov_b32_e32 v32, v131
	v_mov_b32_e32 v33, v132
	v_smfmac_f32_16x16x64_f16 v[62:65], v[4:7], a[8:15], v28
	v_smfmac_f32_16x16x64_f16 v[66:69], v[4:7], a[136:143], v28
	global_load_ushort v128, v[114:115], off
	v_smfmac_f32_16x16x64_f16 v[62:65], v[8:11], a[16:23], v28
	v_smfmac_f32_16x16x64_f16 v[66:69], v[8:11], a[144:151], v28
	global_load_ushort v129, v[114:115], off offset:2048
	v_smfmac_f32_16x16x64_f16 v[62:65], v[12:15], a[24:31], v28
	v_smfmac_f32_16x16x64_f16 v[66:69], v[12:15], a[152:159], v28
	global_load_ushort v130, v[116:117], off
	s_waitcnt lgkmcnt(11)
	v_smfmac_f32_16x16x64_f16 v[62:65], v[50:53], a[32:39], v28
	v_smfmac_f32_16x16x64_f16 v[66:69], v[50:53], a[160:167], v28
	global_load_ushort v131, v[116:117], off offset:2048
	s_waitcnt lgkmcnt(10)
	v_smfmac_f32_16x16x64_f16 v[62:65], v[54:57], a[40:47], v28
	v_smfmac_f32_16x16x64_f16 v[66:69], v[54:57], a[168:175], v28
	global_load_ushort v132, v[118:119], off
	s_waitcnt lgkmcnt(9)
	v_smfmac_f32_16x16x64_f16 v[62:65], v[58:61], a[48:55], v28
	v_smfmac_f32_16x16x64_f16 v[66:69], v[58:61], a[176:183], v28
	global_store_dword v[112:113], v46, off
	s_waitcnt lgkmcnt(8)
	v_smfmac_f32_16x16x64_f16 v[62:65], v[70:73], a[56:63], v28
	v_smfmac_f32_16x16x64_f16 v[66:69], v[70:73], a[184:191], v28
	v_cvt_f32_f16_e32 v112, v44
	v_cvt_f32_f16_e32 v113, v43
	v_cvt_f32_f16_e32 v114, v42
	v_cvt_f32_f16_e32 v115, v41
	v_cvt_f32_f16_e32 v118, v45
	v_cndmask_b32_e64 v116, 0, v118, s[22:23]
	v_cndmask_b32_e64 v117, v118, 0, s[22:23]
	v_add_f32_e32 v113, v113, v116
	v_add_f32_e32 v115, v115, v117
	v_pk_mul_f32 v[112:113], v[112:113], s[40:41]
	v_pk_mul_f32 v[114:115], v[114:115], s[42:43]
	s_waitcnt lgkmcnt(7)
	v_smfmac_f32_16x16x64_f16 v[62:65], v[78:81], a[64:71], v28
	v_smfmac_f32_16x16x64_f16 v[66:69], v[78:81], a[192:199], v28
	s_waitcnt lgkmcnt(6)
	v_smfmac_f32_16x16x64_f16 v[62:65], v[82:85], a[72:79], v28
	v_smfmac_f32_16x16x64_f16 v[66:69], v[82:85], a[200:207], v28
	s_waitcnt lgkmcnt(5)
	v_smfmac_f32_16x16x64_f16 v[62:65], v[86:89], a[80:87], v28
	v_smfmac_f32_16x16x64_f16 v[66:69], v[86:89], a[208:215], v28
	s_waitcnt lgkmcnt(4)
	v_smfmac_f32_16x16x64_f16 v[62:65], v[90:93], a[88:95], v28
	v_smfmac_f32_16x16x64_f16 v[66:69], v[90:93], a[216:223], v28
	s_waitcnt lgkmcnt(3)
	v_smfmac_f32_16x16x64_f16 v[62:65], v[94:97], a[96:103], v28
	v_smfmac_f32_16x16x64_f16 v[66:69], v[94:97], a[224:231], v28
	s_waitcnt lgkmcnt(2)
	v_smfmac_f32_16x16x64_f16 v[62:65], v[98:101], a[104:111], v28
	v_smfmac_f32_16x16x64_f16 v[66:69], v[98:101], a[232:239], v28
	s_waitcnt lgkmcnt(1)
	v_smfmac_f32_16x16x64_f16 v[62:65], v[102:105], a[112:119], v28
	v_smfmac_f32_16x16x64_f16 v[66:69], v[102:105], a[240:247], v28
	s_waitcnt lgkmcnt(0)
	v_smfmac_f32_16x16x64_f16 v[62:65], v[106:109], a[120:127], v28
	v_smfmac_f32_16x16x64_f16 v[66:69], v[106:109], a[248:255], v28
	s_nop 6
	v_permlane32_swap_b32_e32 v62, v63
	v_permlane32_swap_b32_e32 v64, v65
	v_permlane32_swap_b32_e32 v66, v67
	v_permlane32_swap_b32_e32 v68, v69
	v_add_f32_e32 v2, v62, v63
	v_add_f32_e32 v3, v64, v65
	v_add_f32_e32 v6, v66, v67
	v_add_f32_e32 v7, v68, v69
.Lrec_gate2:
	v_cndmask_b32_e64 v4, v2, v3, s[2:3]
	v_cndmask_b32_e64 v5, v6, v7, s[2:3]
	s_nop 0
	v_mov_b32_dpp v2, v4 row_ror:8 row_mask:0xf bank_mask:0xc
	v_mov_b32_dpp v3, v4 row_ror:8 row_mask:0xf bank_mask:0x3
	v_mov_b32_dpp v6, v5 row_ror:8 row_mask:0xf bank_mask:0xc
	v_mov_b32_dpp v7, v5 row_ror:8 row_mask:0xf bank_mask:0x3
	v_pk_fma_f32 v[2:3], v[2:3], s[40:41], v[112:113]
	v_pk_fma_f32 v[6:7], v[6:7], s[42:43], v[114:115]
	v_exp_f32_e32 v2, v2
	v_exp_f32_e32 v6, v6
	v_exp_f32_e32 v3, v3
	v_exp_f32_e32 v7, v7
	s_nop 0
	v_pk_add_f32 v[2:3], v[2:3], s[44:45]
	v_pk_add_f32 v[6:7], v[6:7], s[44:45]
	v_rcp_f32_e32 v6, v6
	v_rcp_f32_e32 v2, v2
	v_rcp_f32_e32 v3, v3
	v_rcp_f32_e32 v7, v7
	v_fma_f32 v0, v6, -2.0, 1.0
	v_mul_f32_e32 v0, v2, v0
	v_fmac_f32_e32 v0, v26, v3
	v_mul_f32_e32 v1, 0x4038aa3b, v0
	v_exp_f32_e32 v1, v1
	s_cmpk_eq_i32 s29, 0x7f
	v_add_f32_e32 v1, 1.0, v1
	v_rcp_f32_e32 v1, v1
	s_nop 0
	v_fma_f32 v1, v1, -2.0, 1.0
	v_mul_f32_e32 v46, v7, v1
	s_cbranch_scc1 .LBB2_29
	v_cvt_f16_f32_e32 v2, v46
	s_cmp_lg_u64 s[0:1], 0
	v_bitop3_b16 v2, s37, v2, -2 bitop3:0xf8
	s_cbranch_scc1 .Lrec_pub_slow
	global_store_short v120, v2, s[8:9]
	s_branch .LBB2_29

.LBB2_23:
	s_mov_b32 s32, 0x4000
	s_mov_b32 s33, 0
	v_lshl_add_u64 v[114:115], v[20:21], 0, s[32:33]
	v_lshl_add_u64 v[118:119], v[22:23], 0, s[32:33]
	v_add_co_u32_e32 v116, vcc, 0x1000, v114
	s_nop 1
	v_addc_co_u32_e32 v117, vcc, 0, v115, vcc
	global_load_ushort v128, v[114:115], off
	global_load_ushort v129, v[114:115], off offset:2048
	global_load_ushort v130, v[116:117], off
	global_load_ushort v131, v[116:117], off offset:2048
	global_load_ushort v132, v[118:119], off
	v_mov_b32_e32 v2, 0
	v_mov_b32_e32 v3, 0
	v_mov_b32_e32 v6, 0
	v_mov_b32_e32 v7, 0
	v_cvt_f32_f16_e32 v112, v44
	v_cvt_f32_f16_e32 v113, v43
	v_cvt_f32_f16_e32 v114, v42
	v_cvt_f32_f16_e32 v115, v41
	v_cvt_f32_f16_e32 v118, v45
	v_cndmask_b32_e64 v116, 0, v118, s[22:23]
	v_cndmask_b32_e64 v117, v118, 0, s[22:23]
	v_add_f32_e32 v113, v113, v116
	v_add_f32_e32 v115, v115, v117
	v_pk_mul_f32 v[112:113], v[112:113], s[40:41]
	v_pk_mul_f32 v[114:115], v[114:115], s[42:43]
	s_branch .Lrec_gate2
